# baseline (speedup 1.0000x reference)
.LBB2_12:
	s_or_b64 exec, exec, s[12:13]
	v_lshlrev_b32_e32 v106, 9, v119
	v_ffbl_b32_e32 v107, v107
	v_ffbl_b32_e32 v108, v108
	v_lshlrev_b32_e32 v116, 25, v119
	v_lshl_or_b32 v107, v107, 4, v106
	v_mov_b32_e32 v109, 0x2000
	v_lshl_or_b32 v108, v108, 20, v116
	v_bfrev_b32_e32 v116, 4
	v_ffbl_b32_e32 v0, v0
	v_cndmask_b32_e64 v107, v107, v109, s[8:9]
	v_cndmask_b32_e64 v108, v108, v116, s[4:5]
	v_lshl_or_b32 v0, v0, 4, v106
	v_cndmask_b32_e32 v0, v0, v109, vcc
	v_or_b32_e32 v106, v108, v107
	v_mov_b32_e32 v108, 0x800000
	v_lshlrev_b32_e32 v107, 16, v117
	v_cndmask_b32_e64 v108, 0, v108, s[6:7]
	s_waitcnt lgkmcnt(2)
	v_lshl_or_b32 v0, v118, 24, v0
	v_or3_b32 v0, v0, v108, v107
	ds_write2_b32 v105, v106, v0 offset0:1 offset1:3
	v_cmp_ne_u32_e32 vcc, 0, v140
	v_cmp_ne_u32_e64 s[22:23], 0, v141
	v_lshlrev_b32_e32 v150, 5, v113
	v_lshl_add_u32 v155, v113, 2, v115
	v_lshlrev_b32_e32 v155, 2, v155
	v_add_u32_e32 v155, 0x11840, v155
	v_lshrrev_b64 v[146:147], v150, vcc
	v_lshrrev_b64 v[156:157], v150, s[22:23]
	v_mov_b32_e32 v151, 0x400
	v_cmp_ne_u32_e32 vcc, 0, v146
	v_cmp_ne_u32_e64 s[22:23], 0, v156
	s_nop 1
	v_cndmask_b32_e32 v146, 0, v151, vcc
	v_cndmask_b32_e64 v156, 0, v151, s[22:23]
	v_cmp_eq_u32_e32 vcc, 0, v111
	s_and_saveexec_b64 s[22:23], vcc
	ds_or_b32 v155, v146
	ds_or_b32 v155, v156 offset:32
	s_or_b64 exec, exec, s[22:23]
	s_movk_i32 s2, 0x2010
	v_mul_u32_u24_e32 v105, 0x2010, v115
	v_cmp_eq_u32_e32 vcc, 0, v114
	s_waitcnt vmcnt(22)
	ds_write_b128 v104, v[38:41] offset:32832
	s_waitcnt vmcnt(21)
	ds_write_b128 v104, v[42:45] offset:36928
	s_waitcnt vmcnt(20)
	ds_write_b128 v104, v[46:49] offset:41024
	s_waitcnt vmcnt(19)
	ds_write_b128 v104, v[50:53] offset:45120
	s_waitcnt vmcnt(18)
	ds_write_b128 v104, v[54:57] offset:49216
	s_waitcnt vmcnt(17)
	ds_write_b128 v104, v[66:69] offset:53312
	s_and_saveexec_b64 s[0:1], vcc
	v_mov_b32_e32 v38, 0
	v_mov_b32_e32 v39, v38
	v_mov_b32_e32 v40, v38
	v_mov_b32_e32 v41, v38
	ds_write_b128 v105, v[38:41] offset:8192
	s_or_b64 exec, exec, s[0:1]
	v_lshlrev_b32_e32 v40, 3, v113
	v_lshlrev_b32_e32 v67, 4, v110
	v_or_b32_e32 v38, 0x1e0, v111
	v_or_b32_e32 v0, 0x8040, v40
	v_mad_u32_u24 v66, v1, s2, v67
	v_mad_u32_u24 v38, v38, 48, v0
	s_waitcnt vmcnt(16)
	ds_write_b128 v66, v[58:61]
	s_waitcnt vmcnt(15)
	ds_write_b128 v66, v[62:65] offset:1024
	s_waitcnt vmcnt(14)
	ds_write_b128 v66, v[70:73] offset:2048
	s_waitcnt vmcnt(13)
	ds_write_b128 v66, v[74:77] offset:3072
	s_waitcnt vmcnt(12)
	ds_write_b128 v66, v[78:81] offset:4096
	s_waitcnt vmcnt(11)
	ds_write_b128 v66, v[82:85] offset:5120
	s_waitcnt vmcnt(10)
	ds_write_b128 v66, v[86:89] offset:6144
	s_waitcnt vmcnt(9)
	ds_write_b128 v66, v[90:93] offset:7168
	s_waitcnt lgkmcnt(0)
	s_barrier
	v_readfirstlane_b32 s31, v115
	s_cmp_eq_u32 s31, 0
	s_cbranch_scc1 .Lstag_done
	s_sleep 4
	s_cmp_eq_u32 s31, 1
	s_cbranch_scc1 .Lstag_done
	s_sleep 4
	s_cmp_eq_u32 s31, 2
	s_cbranch_scc1 .Lstag_done
	s_sleep 4
.Lstag_done:
	v_lshl_add_u32 v116, v113, 3, v105
	v_or_b32_e32 v106, 0x1e0, v111
	v_lshlrev_b32_e32 v138, 4, v106
	v_lshlrev_b32_e32 v139, 3, v106
	v_add_u32_e32 v139, 0x118c0, v139
	v_mul_u32_u24_e32 v156, 48, v106
	v_add_u32_e32 v156, v0, v156
	v_mov_b32_e32 v157, 0x1187c
	v_add_u32_e32 v137, v116, v138
	v_add_u32_e32 v138, 0x200, v138
	v_lshlrev_b32_e32 v160, 4, v111
	v_lshlrev_b32_e32 v161, 3, v111
	v_add_u32_e32 v161, 0x118c0, v161
	v_mul_u32_u24_e32 v162, 48, v111
	v_add_u32_e32 v162, v0, v162
	v_mov_b32_e32 v163, 0x11840
	v_mul_hi_u32_u24_e32 v159, 0x410, v111
	v_mul_u32_u24_e32 v158, 0x410, v111
	v_mov_b32_e32 v107, 0x82000
	v_mad_u64_u32 v[158:159], s[0:1], s20, v107, v[158:159]
	v_lshlrev_b32_e32 v107, 3, v113
	v_or_b32_e32 v158, v158, v107
	v_lshl_add_u64 v[158:159], s[14:15], 0, v[158:159]
	s_mov_b64 s[0:1], 0x79e30
	s_mov_b32 s2, 0xffff7e00
	s_mov_b32 s3, -1
	v_lshl_add_u64 v[158:159], v[158:159], 0, s[0:1]
	ds_read_b128 v[38:41], v138 offset:56896
	ds_read_b64 v[42:43], v139
	ds_read2_b64 v[56:59], v156 offset1:2
	v_lshl_add_u32 v107, v114, 2, v163
	v_add_u32_e32 v107, -8, v107
	ds_read_b32 v60, v107
	v_add_u32_e32 v156, 0xfffffa00, v156
	ds_read2_b64 v[52:55], v156 offset1:2
	v_add_u32_e32 v106, -2, v114
	v_cmp_gt_u32_e32 vcc, 16, v106
	s_waitcnt lgkmcnt(0)
	v_cndmask_b32_e32 v60, 0, v60, vcc
	s_nop 1
	v_readlane_b32 s4, v60, 17
	v_readlane_b32 s21, v60, 16
	v_add_u32_sdwa v92, v105, v56 dst_sel:DWORD dst_unused:UNUSED_PAD src0_sel:DWORD src1_sel:WORD_0
	v_add_u32_sdwa v93, v105, v56 dst_sel:DWORD dst_unused:UNUSED_PAD src0_sel:DWORD src1_sel:WORD_1
	v_add_u32_sdwa v106, v105, v57 dst_sel:DWORD dst_unused:UNUSED_PAD src0_sel:DWORD src1_sel:WORD_0
	v_add_u32_sdwa v107, v105, v57 dst_sel:DWORD dst_unused:UNUSED_PAD src0_sel:DWORD src1_sel:WORD_1
	v_add_u32_sdwa v108, v105, v58 dst_sel:DWORD dst_unused:UNUSED_PAD src0_sel:DWORD src1_sel:WORD_0
	v_add_u32_sdwa v109, v105, v58 dst_sel:DWORD dst_unused:UNUSED_PAD src0_sel:DWORD src1_sel:WORD_1
	v_add_u32_sdwa v88, v105, v59 dst_sel:DWORD dst_unused:UNUSED_PAD src0_sel:DWORD src1_sel:WORD_0
	v_add_u32_sdwa v89, v105, v59 dst_sel:DWORD dst_unused:UNUSED_PAD src0_sel:DWORD src1_sel:WORD_1
	ds_read_b128 v[120:123], v92
	ds_read_b128 v[124:127], v93
	ds_read_b128 v[128:131], v106
	ds_read_b128 v[132:135], v107
	ds_read_b128 v[140:143], v108
	ds_read_b128 v[144:147], v109
	ds_read_b128 v[148:151], v88
	ds_read_b128 v[152:155], v89
	s_waitcnt lgkmcnt(0)
	v_pk_add_f32 v[120:121], v[120:121], v[124:125]
	v_pk_add_f32 v[122:123], v[122:123], v[126:127]
	v_pk_add_f32 v[128:129], v[128:129], v[132:133]
	v_pk_add_f32 v[130:131], v[130:131], v[134:135]
	v_pk_add_f32 v[140:141], v[140:141], v[144:145]
	v_pk_add_f32 v[142:143], v[142:143], v[146:147]
	v_pk_add_f32 v[148:149], v[148:149], v[152:153]
	v_pk_add_f32 v[150:151], v[150:151], v[154:155]
	s_bitcmp1_b32 s4, 8
	s_cbranch_scc1 .Lfarslow_pre
